# static priority for waves 4-7 also in prep and SGU spatial phases
# speedup vs baseline: 1.0097x; 1.0005x over previous
.LBB0_301:
	s_cmp_lt_i32 s92, 4
	s_cselect_b64 s[4:5], -1, 0
	s_cmp_gt_i32 s93, 3
	s_cselect_b64 s[6:7], -1, 0
	s_and_b64 s[4:5], s[4:5], s[6:7]
	s_andn2_b64 vcc, exec, s[4:5]
	s_cbranch_vccnz .LBB0_441
	s_cmp_lt_u32 s88, 4
	s_cbranch_scc1 .Lmy_prio_skip3
	s_setprio 2
.Lmy_prio_skip3:
	s_cmpk_gt_i32 s89, 0x21f
	s_cbranch_scc1 .LBB0_391
	s_add_u32 s3, s26, 0x21d00000
	s_addc_u32 s22, s27, 0
	s_add_u32 s10, s26, 0x580000
	s_addc_u32 s11, s27, 0
	s_add_u32 s23, s26, 0x23f00000
	s_addc_u32 s30, s27, 0
	s_lshl_b32 s31, s88, 4
	s_add_u32 s35, s26, 0x37100000
	s_addc_u32 s36, s27, 0
	s_add_u32 s37, s26, 0x32d00000
	s_addc_u32 s40, s27, 0
	s_lshl_b32 s4, s88, 3
	s_mov_b32 s5, 0
	s_lshl_b64 s[4:5], s[4:5], 10
	v_and_b32_e32 v1, 15, v250
	s_add_u32 s8, s26, s4
	v_and_b32_e32 v5, -16, v250
	v_mul_u32_u24_e32 v6, 0x210, v1
	s_addc_u32 s9, s27, s5
	s_lshl_b32 s12, s88, 11
	v_ashrrev_i32_e32 v4, 4, v250
	v_add3_u32 v123, 0, v5, v6
	v_lshlrev_b32_e32 v5, 2, v250
	v_lshlrev_b32_e32 v34, 3, v4
	v_lshlrev_b32_e32 v4, 2, v4
	v_and_b32_e32 v5, 0xffffff80, v5
	v_lshl_or_b32 v6, v1, 3, s12
	v_and_b32_e32 v4, 4, v4
	v_add_u32_e32 v7, v6, v5
	v_or_b32_e32 v36, v7, v4
	v_add_u32_e32 v7, 0x100, v5
	v_add_u32_e32 v8, v7, v6
	v_or_b32_e32 v38, v8, v4
	v_or_b32_e32 v8, 0x200, v6
	v_add_u32_e32 v9, v8, v5
	v_add_u32_e32 v8, v8, v7
	v_or_b32_e32 v42, v8, v4
	v_or_b32_e32 v8, 0x400, v6
	v_or_b32_e32 v6, 0x600, v6
	v_lshlrev_b32_e32 v2, 3, v250
	v_or_b32_e32 v40, v9, v4
	v_add_u32_e32 v9, v8, v5
	v_add_u32_e32 v5, v6, v5
	v_ashrrev_i32_e32 v3, 31, v2
	v_add_u32_e32 v8, v8, v7
	v_or_b32_e32 v48, v5, v4
	v_add_u32_e32 v5, v6, v7
	s_movk_i32 s4, 0x400
	s_movk_i32 s41, 0x1000
	v_or_b32_e32 v44, v9, v4
	v_or_b32_e32 v46, v8, v4
	v_or_b32_e32 v50, v5, v4
	v_lshl_add_u64 v[2:3], v[2:3], 1, s[8:9]
	s_mov_b64 s[8:9], 0x34f00000
	v_cmp_gt_i32_e64 s[4:5], s4, v170
	v_ashrrev_i32_e32 v35, 31, v34
	v_cmp_gt_i32_e64 s[6:7], s41, v170
	v_and_b32_e32 v122, 3, v170
	s_movk_i32 s42, 0x210
	v_ashrrev_i32_e32 v37, 31, v36
	v_ashrrev_i32_e32 v39, 31, v38
	v_ashrrev_i32_e32 v41, 31, v40
	v_ashrrev_i32_e32 v43, 31, v42
	v_ashrrev_i32_e32 v45, 31, v44
	v_ashrrev_i32_e32 v47, 31, v46
	v_ashrrev_i32_e32 v49, 31, v48
	v_ashrrev_i32_e32 v51, 31, v50
	v_lshl_add_u64 v[52:53], v[2:3], 0, s[8:9]
	v_lshlrev_b32_e32 v124, 3, v170
	v_mov_b32_e32 v55, 0
	s_mov_b32 s43, 0xffff0000
	s_movk_i32 s44, 0x7fff
	s_movk_i32 s45, 0x1ff
	s_mov_b32 s46, 0x5040100
	s_movk_i32 s47, 0xdff
	s_mov_b32 s12, s89
	s_branch .LBB0_305

.LBB0_441:
	s_setprio 0
	s_cmp_lt_i32 s92, 5
	s_cselect_b64 s[4:5], -1, 0
	s_cmp_gt_i32 s93, 4
	s_cselect_b64 s[6:7], -1, 0
	s_and_b64 s[4:5], s[4:5], s[6:7]
	s_andn2_b64 vcc, exec, s[4:5]
	s_cbranch_vccnz .LBB0_527
	s_cmp_lt_u32 s88, 4
	s_cbranch_scc1 .Lmy_prio_skip4
	s_setprio 2

.LBB0_1859:
	s_cmp_lt_i32 s92, 25
	s_cselect_b64 s[4:5], -1, 0
	s_cmp_gt_i32 s93, 24
	s_cselect_b64 s[6:7], -1, 0
	s_and_b64 s[4:5], s[4:5], s[6:7]
	s_andn2_b64 vcc, exec, s[4:5]
	s_mov_b32 s4, 24
	s_cbranch_vccnz .LBB0_1921
	s_cmp_lt_u32 s88, 4
	s_cbranch_scc1 .Lmy_prio_skip24
	s_setprio 2
.Lmy_prio_skip24:
	s_cmpk_gt_i32 s89, 0xcbf
	s_mov_b32 s6, 22
	s_cbranch_scc1 .LBB0_1871
	s_add_u32 s3, s26, 0x21d00000
	s_addc_u32 s22, s27, 0
	s_add_u32 s23, s26, 0x28500000
	s_addc_u32 s28, s27, 0
	s_add_u32 s29, s26, 0x32d00000
	s_addc_u32 s30, s27, 0
	s_add_u32 s31, s26, 0x500000
	s_addc_u32 s33, s27, 0
	s_ashr_i32 s7, s6, 31
	s_lshl_b64 s[6:7], s[6:7], 3
	s_add_u32 s6, s0, s6
	s_addc_u32 s7, s1, s7
	s_ashr_i32 s5, s4, 31
	s_lshl_b64 s[4:5], s[4:5], 3
	s_add_u32 s4, s0, s4
	s_addc_u32 s5, s1, s5
	s_load_dwordx2 s[8:9], s[6:7], 0x0
	s_load_dwordx2 s[10:11], s[4:5], 0x0
	s_lshl_b32 s4, s88, 5
	s_add_i32 s12, s4, 0
	s_waitcnt vmcnt(0)
	v_ashrrev_i32_e32 v2, 4, v250
	s_add_i32 s6, 0, 0x11000
	s_lshl_b32 s13, s88, 6
	v_lshlrev_b32_e32 v20, 3, v2
	v_and_b32_e32 v3, -16, v250
	s_waitcnt lgkmcnt(0)
	s_add_u32 s8, s8, s13
	v_lshlrev_b32_e32 v2, 2, v2
	v_and_b32_e32 v1, 15, v250
	v_add_u32_e32 v4, 0, v3
	s_addc_u32 s9, s9, 0
	v_ashrrev_i32_e32 v3, 31, v2
	s_movk_i32 s4, 0x80
	v_ashrrev_i32_e32 v171, 31, v170
	v_lshl_add_u32 v26, v170, 2, s6
	s_movk_i32 s6, 0x800
	v_lshl_add_u64 v[22:23], v[2:3], 2, s[8:9]
	v_add_u32_e32 v2, s12, v20
	v_mul_u32_u24_e32 v3, 0x110, v1
	v_cmp_gt_i32_e64 s[4:5], s4, v170
	v_lshl_add_u64 v[18:19], v[170:171], 2, s[96:97]
	v_lshl_or_b32 v27, s88, 4, v1
	v_ashrrev_i32_e32 v21, 31, v20
	v_cmp_gt_i32_e64 s[6:7], s6, v170
	s_movk_i32 s36, 0x110
	v_lshlrev_b32_e32 v28, 3, v170
	v_mov_b32_e32 v29, 0x358637bd
	s_mov_b32 s37, 0xf800000
	v_mov_b32_e32 v30, 0x260
	v_mov_b32_e32 v25, 0
	s_movk_i32 s40, 0x5ff
	v_add_u32_e32 v31, v4, v3
	v_add_u32_e32 v32, v2, v3
	s_movk_i32 s41, 0x1800
	v_and_b32_e32 v197, 0x7f, v170
	v_lshlrev_b32_e32 v197, 2, v197
	s_mov_b32 s101, s89
	s_mul_hi_i32 s48, s101, 0x2aaaaaab
	s_ashr_i32 s48, s48, 2
	v_lshl_add_u32 v196, s48, 9, v197
	global_load_dword v172, v196, s[96:97]
	v_add_u32_e32 v199, 0x11000, v196
	global_load_dword v173, v199, s[96:97]
	v_add_u32_e32 v198, 0x22000, v196
	global_load_dword v174, v198, s[96:97]
	v_add_u32_e32 v199, 0x33000, v196
	global_load_dword v175, v199, s[96:97]
	v_add_u32_e32 v198, 0x44000, v196
	global_load_dword v176, v198, s[96:97]
	v_add_u32_e32 v199, 0x55000, v196
	global_load_dword v177, v199, s[96:97]
	v_add_u32_e32 v198, 0x66000, v196
	global_load_dword v178, v198, s[96:97]
	v_add_u32_e32 v199, 0x77000, v196
	global_load_dword v179, v199, s[96:97]
	v_add_u32_e32 v198, 0x88000, v196
	global_load_dword v180, v198, s[96:97]
	v_add_u32_e32 v199, 0x99000, v196
	global_load_dword v181, v199, s[96:97]
	v_add_u32_e32 v198, 0xaa000, v196
	global_load_dword v182, v198, s[96:97]
	v_add_u32_e32 v199, 0xbb000, v196
	global_load_dword v183, v199, s[96:97]
	v_add_u32_e32 v198, 0xcc000, v196
	global_load_dword v184, v198, s[96:97]
	v_add_u32_e32 v199, 0xdd000, v196
	global_load_dword v185, v199, s[96:97]
	v_add_u32_e32 v198, 0xee000, v196
	global_load_dword v186, v198, s[96:97]
	v_add_u32_e32 v199, 0xff000, v196
	global_load_dword v187, v199, s[96:97]
	v_add_u32_e32 v198, 0x110000, v196
	global_load_dword v188, v198, s[96:97]
	v_add_u32_e32 v199, 0x121000, v196
	global_load_dword v189, v199, s[96:97]
	v_add_u32_e32 v198, 0x132000, v196
	global_load_dword v190, v198, s[96:97]
	v_add_u32_e32 v199, 0x143000, v196
	global_load_dword v191, v199, s[96:97]
	v_add_u32_e32 v198, 0x154000, v196
	global_load_dword v192, v198, s[96:97]
	v_add_u32_e32 v199, 0x165000, v196
	global_load_dword v193, v199, s[96:97]
	v_add_u32_e32 v198, 0x176000, v196
	global_load_dword v194, v198, s[96:97]
	v_add_u32_e32 v199, 0x187000, v196
	global_load_dword v195, v199, s[96:97]
	s_mul_hi_i32 s46, s101, 0x2aaaaaab
	s_lshr_b32 s47, s46, 31
	s_ashr_i32 s48, s46, 2
	s_add_i32 s48, s48, s47
	s_mul_i32 s53, s48, 0xffffffe8
	s_add_i32 s53, s53, s101
	s_mul_hi_i32 s54, s53, 0x55555556
	s_mul_i32 s55, s54, -3
	s_add_i32 s55, s55, s53
	s_lshl_b32 s55, s55, 7
	s_mul_i32 s53, s54, 0x180
	s_add_i32 s55, s55, s53
	v_lshlrev_b32_e32 v244, 4, v170
	v_lshl_add_u32 v244, s54, 15, v244
	v_mov_b32_e32 v247, s33
	v_add_co_u32_e32 v246, vcc, s31, v244
	s_nop 1
	v_addc_co_u32_e32 v247, vcc, 0, v247, vcc
	global_load_dwordx4 v[200:203], v[246:247], off
	v_add_co_u32_e32 v246, vcc, 0x2000, v246
	s_nop 1
	v_addc_co_u32_e32 v247, vcc, 0, v247, vcc
	global_load_dwordx4 v[204:207], v[246:247], off
	v_add_co_u32_e32 v246, vcc, 0x2000, v246
	s_nop 1
	v_addc_co_u32_e32 v247, vcc, 0, v247, vcc
	global_load_dwordx4 v[208:211], v[246:247], off
	v_add_co_u32_e32 v246, vcc, 0x2000, v246
	s_nop 1
	v_addc_co_u32_e32 v247, vcc, 0, v247, vcc
	global_load_dwordx4 v[212:215], v[246:247], off
	v_lshl_or_b32 v245, s54, 7, v1
	v_lshlrev_b32_e32 v245, 2, v245
	global_load_dword v216, v245, s[10:11]
	global_load_dword v217, v245, s[10:11] offset:64
	global_load_dword v218, v245, s[10:11] offset:128
	global_load_dword v219, v245, s[10:11] offset:192
	global_load_dword v220, v245, s[10:11] offset:256
	global_load_dword v221, v245, s[10:11] offset:320
	global_load_dword v222, v245, s[10:11] offset:384
	global_load_dword v223, v245, s[10:11] offset:448
	v_mov_b32_e32 v248, s55
	v_mov_b32_e32 v249, 0
	v_lshl_add_u64 v[248:249], v[248:249], 2, v[22:23]
	global_load_dwordx4 v[224:227], v[248:249], off
	s_mul_i32 s46, s48, 0xffffffe8
	s_add_i32 s46, s46, s101
	s_mul_hi_i32 s47, s46, 0x55555556
	s_lshr_b32 s51, s47, 31
	s_add_i32 s52, s47, s51
	s_mul_i32 s47, s52, -3
	s_add_i32 s47, s47, s46
	s_mul_i32 s46, s52, 0x180
	s_lshl_b32 s47, s47, 7
	s_add_i32 s46, s47, s46
	s_mul_hi_i32 s47, s48, 0xc0000
	s_mul_i32 s48, s48, 0xc0000
	v_add_u32_e32 v252, s46, v27
	s_add_u32 s48, s23, s48
	v_ashrrev_i32_e32 v253, 31, v252
	s_addc_u32 s49, s28, s47
	v_lshlrev_b64 v[252:253], 8, v[252:253]
	v_lshl_add_u64 v[252:253], s[48:49], 0, v[252:253]
	v_lshl_add_u64 v[252:253], v[20:21], 1, v[252:253]
	global_load_dwordx4 v[240:243], v[252:253], off
	global_load_dwordx4 v[236:239], v[252:253], off offset:64
	global_load_dwordx4 v[232:235], v[252:253], off offset:128
	s_nop 0
	global_load_dwordx4 v[228:231], v[252:253], off offset:192
	s_waitcnt vmcnt(0)
	s_mov_b32 s42, s89
	s_branch .LBB0_1863

.LBB0_1921:
	s_setprio 0
	s_cmp_lt_i32 s92, 26
	s_cselect_b64 s[4:5], -1, 0
	s_cmp_gt_i32 s93, 25
	s_cselect_b64 s[6:7], -1, 0
	s_and_b64 s[4:5], s[4:5], s[6:7]
	s_andn2_b64 vcc, exec, s[4:5]
	s_cbranch_vccnz .LBB0_2013
	s_waitcnt vmcnt(0)
	v_mov_b32_e32 v6, v0
	s_cmpk_gt_i32 s2, 0xff
	v_readfirstlane_b32 s14, v6
	s_cbranch_scc0 .LBB0_1928
	s_mov_b64 s[6:7], 0
	s_cmpk_lt_u32 s2, 0x1c0
	s_mov_b64 s[4:5], 0
	s_cbranch_scc0 .LBB0_1925
	s_and_b32 s3, s2, 0xff
	s_mulk_i32 s3, 0xab
	s_lshr_b32 s4, s3, 11
	s_mul_i32 s4, s4, 12
	s_sub_i32 s4, s2, s4
	s_and_b32 s40, s4, 0xff
	s_bfe_u32 s68, s3, 0x2000b
	s_lshr_b32 s33, s3, 13
	s_mov_b64 s[4:5], -1
	s_and_b64 vcc, exec, s[6:7]
	s_cbranch_vccz .LBB0_1929
	s_branch .LBB0_1926

.LBB0_2359:
	s_cmp_lt_i32 s92, 32
	s_cselect_b64 s[4:5], -1, 0
	s_cmp_gt_i32 s93, 31
	s_cselect_b64 s[6:7], -1, 0
	s_and_b64 s[4:5], s[4:5], s[6:7]
	s_andn2_b64 vcc, exec, s[4:5]
	s_cbranch_vccnz .LBB0_2499
	s_cmp_lt_u32 s88, 4
	s_cbranch_scc1 .Lmy_prio_skip31
	s_setprio 2
.Lmy_prio_skip31:
	s_cmpk_gt_i32 s89, 0x21f
	s_cbranch_scc1 .LBB0_2449
	s_add_u32 s3, s26, 0x21d00000
	s_addc_u32 s22, s27, 0
	s_add_u32 s10, s26, 0x580000
	s_addc_u32 s11, s27, 0
	s_add_u32 s23, s26, 0x23f00000
	s_addc_u32 s30, s27, 0
	s_lshl_b32 s31, s88, 4
	s_add_u32 s36, s26, 0x37100000
	s_addc_u32 s37, s27, 0
	s_add_u32 s40, s26, 0x32d00000
	s_addc_u32 s41, s27, 0
	s_lshl_b32 s4, s88, 3
	s_mov_b32 s5, 0
	s_lshl_b64 s[4:5], s[4:5], 10
	v_and_b32_e32 v1, 15, v250
	s_add_u32 s8, s26, s4
	s_waitcnt vmcnt(0)
	v_and_b32_e32 v5, -16, v250
	v_mul_u32_u24_e32 v6, 0x210, v1
	s_addc_u32 s9, s27, s5
	s_lshl_b32 s12, s88, 11
	v_ashrrev_i32_e32 v4, 4, v250
	v_add3_u32 v123, 0, v5, v6
	v_lshlrev_b32_e32 v5, 2, v250
	v_lshlrev_b32_e32 v34, 3, v4
	v_lshlrev_b32_e32 v4, 2, v4
	v_and_b32_e32 v5, 0xffffff80, v5
	v_lshl_or_b32 v6, v1, 3, s12
	v_and_b32_e32 v4, 4, v4
	v_add_u32_e32 v7, v6, v5
	v_or_b32_e32 v36, v7, v4
	v_add_u32_e32 v7, 0x100, v5
	v_add_u32_e32 v8, v7, v6
	v_or_b32_e32 v38, v8, v4
	v_or_b32_e32 v8, 0x200, v6
	v_add_u32_e32 v9, v8, v5
	v_add_u32_e32 v8, v8, v7
	v_or_b32_e32 v42, v8, v4
	v_or_b32_e32 v8, 0x400, v6
	v_or_b32_e32 v6, 0x600, v6
	v_lshlrev_b32_e32 v2, 3, v250
	v_or_b32_e32 v40, v9, v4
	v_add_u32_e32 v9, v8, v5
	v_add_u32_e32 v5, v6, v5
	v_ashrrev_i32_e32 v3, 31, v2
	v_add_u32_e32 v8, v8, v7
	v_or_b32_e32 v48, v5, v4
	v_add_u32_e32 v5, v6, v7
	s_movk_i32 s4, 0x400
	s_movk_i32 s42, 0x1000
	v_or_b32_e32 v44, v9, v4
	v_or_b32_e32 v46, v8, v4
	v_or_b32_e32 v50, v5, v4
	v_lshl_add_u64 v[2:3], v[2:3], 1, s[8:9]
	s_mov_b64 s[8:9], 0x34f00000
	v_cmp_gt_i32_e64 s[4:5], s4, v170
	v_ashrrev_i32_e32 v35, 31, v34
	v_cmp_gt_i32_e64 s[6:7], s42, v170
	v_and_b32_e32 v122, 3, v170
	s_movk_i32 s43, 0x210
	v_ashrrev_i32_e32 v37, 31, v36
	v_ashrrev_i32_e32 v39, 31, v38
	v_ashrrev_i32_e32 v41, 31, v40
	v_ashrrev_i32_e32 v43, 31, v42
	v_ashrrev_i32_e32 v45, 31, v44
	v_ashrrev_i32_e32 v47, 31, v46
	v_ashrrev_i32_e32 v49, 31, v48
	v_ashrrev_i32_e32 v51, 31, v50
	v_lshl_add_u64 v[52:53], v[2:3], 0, s[8:9]
	v_lshlrev_b32_e32 v124, 3, v170
	v_mov_b32_e32 v55, 0
	s_mov_b32 s44, 0xffff0000
	s_movk_i32 s45, 0x7fff
	s_movk_i32 s46, 0x1ff
	s_mov_b32 s47, 0x5040100
	s_movk_i32 s48, 0xdff
	s_mov_b32 s12, s89
	s_branch .LBB0_2363

.LBB0_2499:
	s_setprio 0
	s_cmp_lt_i32 s92, 33
	s_cselect_b64 s[4:5], -1, 0
	s_cmp_gt_i32 s93, 32
	s_cselect_b64 s[6:7], -1, 0
	s_and_b64 s[4:5], s[4:5], s[6:7]
	s_andn2_b64 vcc, exec, s[4:5]
	s_cbranch_vccnz .LBB0_2587
	s_cmp_lt_u32 s88, 4
	s_cbranch_scc1 .Lmy_prio_skip32
	s_setprio 2
